# v6 + attention units mapped so one XCD takes all query blocks of two heads (K/V tiles stay in that L2)
# speedup vs baseline: 1.0340x; 1.0051x over previous
.LBB0_707:
	s_andn2_b64 vcc, exec, s[8:9]
	s_mov_b32 s60, s2
	s_cmpk_lg_i32 s3, 0x100
	s_cbranch_scc1 .Lxcdmap_1
	s_and_b32 s60, s2, 7
	s_lshl_b32 s60, s60, 5
	s_lshr_b32 s46, s2, 3
	s_or_b32 s60, s60, s46
.Lxcdmap_1:
	s_cbranch_vccz .LBB0_709
	s_branch .LBB0_706

.LBB0_1035:
	s_andn2_b64 vcc, exec, s[0:1]
	s_mov_b32 s21, s2
	s_cmpk_lg_i32 s3, 0x100
	s_cbranch_scc1 .Lxcdmap_2
	s_and_b32 s21, s2, 7
	s_lshl_b32 s21, s21, 5
	s_lshr_b32 s14, s2, 3
	s_or_b32 s21, s21, s14

.LBB0_2890:
	s_and_b64 vcc, exec, s[4:5]
	s_mov_b32 s64, s2
	s_cmpk_lg_i32 s3, 0x100
	s_cbranch_scc1 .Lxcdmap_3
	s_and_b32 s64, s2, 7
	s_lshl_b32 s64, s64, 5
	s_lshr_b32 s50, s2, 3
	s_or_b32 s64, s64, s50

.LBB0_3203:
	s_andn2_b64 vcc, exec, s[0:1]
	s_mov_b32 s20, s2
	s_cmpk_lg_i32 s3, 0x100
	s_cbranch_scc1 .Lxcdmap_4
	s_and_b32 s20, s2, 7
	s_lshl_b32 s20, s20, 5
	s_lshr_b32 s21, s2, 3
	s_or_b32 s20, s20, s21
